# v26 + guards (tail scheme only when grid >= 224 WGs; XCD permutation only inside complete 32-blocks)
# speedup vs baseline: 1.0035x; 1.0035x over previous
; #define LAS __attribute__((address_space(3)))
; __device__ __forceinline__ int opaque_tid() { int t = threadIdx.x; asm volatile("" : "+v"(t)); return t; }
;     __device__ __forceinline__ bool next(int i, Unit& u) const {
;         int U = i * G + c, e = 0, found = 0, rem = 0;
; __device__ __forceinline__ void seg_to_lds(const Args& a, LAS unsigned char* lds, int layer) {
;     LAS int* seg = (LAS int*)(lds + SEG_OFF);
;     const int t = opaque_tid();
;     if (t < 16) {
;         unsigned* cnt = (unsigned*)(a.ws + WS_CTL) + CW_CNT + layer * 16 * 64;
;         const int c = (int)__hip_atomic_load(cnt + t * 64, __ATOMIC_RELAXED, __HIP_MEMORY_SCOPE_AGENT);
;         const int pad = (c + 255) & ~255;
;         int incl = pad;
; #pragma unroll
;         for (int o2 = 1; o2 < 16; o2 <<= 1) { const int u2 = __shfl_up(incl, o2); if (t >= o2) incl += u2; }
;         seg[t] = c; seg[16 + t] = incl - pad;
;         if (t == 15) seg[32] = incl;
;     }
;     __syncthreads();
; }
.LBB0_898:
	s_or_b64 exec, exec, s[36:37]
	s_nop 1
	v_writelane_b32 v254, s61, 61
	s_nop 1
	s_or_b32 vcc_lo, s61, 31
	s_cmp_lt_u32 vcc_lo, s77
	s_cbranch_scc0 .Lxcd_perm_skip_both
	s_and_b32 vcc_lo, s61, 7
	s_lshl_b32 vcc_lo, vcc_lo, 2
	s_lshr_b32 vcc_hi, s61, 3
	s_and_b32 vcc_hi, vcc_hi, 3
	s_or_b32 vcc_lo, vcc_lo, vcc_hi
	s_andn2_b32 s61, s61, 31
	s_or_b32 s61, s61, vcc_lo
	s_add_u32 vcc_lo, s61, s77
	s_nop 1
	v_writelane_b32 v253, vcc_lo, 31
	s_nop 1
.Lxcd_perm_skip_both:
.Lgu_restart:
	v_mov_b32_e32 v1, v0
	s_waitcnt lgkmcnt(0)
	s_barrier
	s_nop 0
	v_cmp_gt_i32_e32 vcc, 16, v1
	s_and_saveexec_b64 s[4:5], vcc
	s_cbranch_execz .LBB0_901
	v_lshlrev_b32_e32 v2, 6, v1
	v_readlane_b32 s6, v254, 22
	v_ashrrev_i32_e32 v3, 31, v2
	v_readlane_b32 s7, v254, 23
	v_cmp_lt_i32_e32 vcc, v235, v240
	s_nop 0
	v_lshl_add_u64 v[2:3], v[2:3], 2, s[6:7]
	global_load_dword v3, v[2:3], off sc1
	s_waitcnt vmcnt(0)
	v_add_u32_e32 v2, 0xff, v3
	v_and_b32_e32 v4, 0xffffff00, v2
	v_cndmask_b32_e32 v2, v235, v199, vcc
	v_lshlrev_b32_e32 v2, 2, v2
	ds_bpermute_b32 v2, v2, v4
	v_cmp_lt_i32_e32 vcc, 0, v1
	s_waitcnt lgkmcnt(0)
	s_nop 0
	v_cndmask_b32_e32 v2, 0, v2, vcc
	v_cmp_lt_i32_e32 vcc, v233, v240
	v_add_u32_e32 v2, v4, v2
	s_nop 0
	v_cndmask_b32_e32 v5, v233, v199, vcc
	v_lshlrev_b32_e32 v5, 2, v5
	ds_bpermute_b32 v5, v5, v2
	v_cmp_lt_i32_e32 vcc, 1, v1
	s_waitcnt lgkmcnt(0)
	s_nop 0
	v_cndmask_b32_e32 v5, 0, v5, vcc
	v_cmp_lt_i32_e32 vcc, v243, v240
	v_add_u32_e32 v2, v2, v5
	s_nop 0
	v_cndmask_b32_e32 v5, v243, v199, vcc
	v_lshlrev_b32_e32 v5, 2, v5
	ds_bpermute_b32 v5, v5, v2
	v_cmp_lt_i32_e32 vcc, 3, v1
	s_waitcnt lgkmcnt(0)
	s_nop 0
	v_cndmask_b32_e32 v5, 0, v5, vcc
	v_cmp_lt_i32_e32 vcc, v203, v240
	v_add_u32_e32 v2, v2, v5
	s_nop 0
	v_cndmask_b32_e32 v5, v203, v199, vcc
	v_lshlrev_b32_e32 v5, 2, v5
	ds_bpermute_b32 v5, v5, v2
	v_cmp_lt_i32_e32 vcc, 7, v1
	s_waitcnt lgkmcnt(0)
	s_nop 0
	v_cndmask_b32_e32 v5, 0, v5, vcc
	v_add_u32_e32 v2, v2, v5
	v_lshl_add_u32 v5, v1, 2, 0
	v_add_u32_e32 v5, 0x21e00, v5
	v_sub_u32_e32 v4, v2, v4
	v_cmp_eq_u32_e32 vcc, 15, v1
	ds_write2_b32 v5, v3, v4 offset1:16
	s_and_b64 exec, exec, vcc
	s_cbranch_execz .LBB0_901
	v_readlane_b32 s2, v253, 58
	s_nop 1
	v_mov_b32_e32 v1, s2
	ds_write_b32 v1, v2

; #define LAS __attribute__((address_space(3)))
;     __device__ __forceinline__ bool next(int i, Unit& u) const {
;         int U = i * G + c, e = 0, found = 0, rem = 0;
;         typedef int i32x4 __attribute__((ext_vector_type(4)));
;         const i32x4 c0 = *(const LAS i32x4*)(seg), c1 = *(const LAS i32x4*)(seg + 4), c2 = *(const LAS i32x4*)(seg + 8), c3 = *(const LAS i32x4*)(seg + 12);
; #pragma unroll
;         for (int k = 0; k < 16; ++k) { const int ck = k < 4 ? c0[k & 3] : k < 8 ? c1[k & 3] : k < 12 ? c2[k & 3] : c3[k & 3];
;             const int nu = ((ck + 255) >> 8) * nct; if (!found) { if (U < nu) { found = 1; e = k; rem = U; } else U -= nu; } }
; template <class Epi, class Sched>
; __device__ __forceinline__ void gemm_phase_gather(LAS unsigned char* lds, const int K, const Sched& S, const Epi& E, const char* Ag, const int* list, const LAS int* seg) {
;     ...
;         Unit nx2; const bool has_nx2 = has_next && S.next(ui + 2, nx2);
.LBB0_1039:
	s_mov_b64 s[8:9], 0
	s_and_b64 vcc, exec, s[20:21]
	s_cbranch_vccz .LBB0_1101
	v_mov_b32_e32 v34, s42
	ds_read_b128 v[134:137], v34
	s_add_i32 s4, s49, 2
	s_mul_i32 s4, s4, s77
	s_add_i32 s5, s4, s61
	s_lshl_b32 s4, s77, 2
	s_cmpk_lt_u32 s77, 0xe0
	s_cselect_b32 s4, 0x7fffffff, s4
	s_cmp_lt_u32 s5, s4
	s_cselect_b32 s5, s5, 0x100000
	v_readlane_b32 s4, v253, 59
	s_mov_b64 s[56:57], s[84:85]
	s_waitcnt lgkmcnt(0)
	v_readfirstlane_b32 s85, v136
	v_mov_b32_e32 v34, s4
	v_readfirstlane_b32 s84, v137
	ds_read_b128 v[136:139], v34
	v_readlane_b32 s4, v253, 60
	v_readfirstlane_b32 s8, v135
	s_waitcnt lgkmcnt(0)
	v_readfirstlane_b32 s63, v136
	v_mov_b32_e32 v34, s4
	v_readfirstlane_b32 s62, v137
	v_readfirstlane_b32 s95, v138
	v_readfirstlane_b32 s94, v139
	ds_read_b128 v[136:139], v34
	v_readlane_b32 s4, v253, 61
	s_waitcnt lgkmcnt(0)
	v_readfirstlane_b32 s79, v136
	v_mov_b32_e32 v34, s4
	v_readfirstlane_b32 s4, v134
	s_addk_i32 s4, 0xff
	s_ashr_i32 s4, s4, 6
	v_readfirstlane_b32 s78, v137
	v_readfirstlane_b32 s75, v138
	v_readfirstlane_b32 s41, v139
	ds_read_b128 v[136:139], v34
	s_and_b32 s9, s4, -4
	s_cmp_lt_i32 s5, s9
	s_cselect_b64 s[6:7], -1, 0
	s_and_b64 vcc, s[6:7], exec
	s_cselect_b32 s6, 0, s9
	s_waitcnt lgkmcnt(0)
	v_readfirstlane_b32 s40, v136
	v_readfirstlane_b32 s39, v137
	v_readfirstlane_b32 s38, v138
	v_readfirstlane_b32 s36, v139
	s_mov_b32 s4, 0
	s_sub_i32 s37, s5, s6
	s_mov_b64 s[6:7], 0
	s_cbranch_vccnz .LBB0_1052
	s_addk_i32 s8, 0xff
	s_ashr_i32 s4, s8, 6
	s_and_b32 s4, s4, -4
	s_cmp_lt_i32 s37, s4
	s_cbranch_scc1 .LBB0_1053
	s_sub_i32 s37, s37, s4
	s_mov_b32 s4, 0
	s_mov_b32 s5, 0
	s_branch .LBB0_1054

; #define LAS __attribute__((address_space(3)))
; __device__ __forceinline__ void gu_mfma(const Args& a, LAS unsigned char* lds, int layer) {
;     seg_to_lds(a, lds, layer);
;     const LAS int* seg = (const LAS int*)(lds + SEG_OFF);
;     pg8::GroupedOrder So{(const char*)(a.ws + WS_HS), (const char*)(a.ws + WS_WGU + (size_t)layer * NE * 1024 * D * 2), seg, 4, (int)gridDim.x, (int)blockIdx.x, (size_t)D * 2, (size_t)1024 * D * 2, (size_t)256 * D * 2};
;     EpiGU E{(bf16_t*)(a.ws + WS_HID), seg};
;     pg8::gemm_phase_gather<EpiGU, pg8::GroupedOrder>(lds, D, So, E, (const char*)(a.ws + WS_ACT), (const int*)(a.ws + WS_LIST), seg);
; }
; __device__ __forceinline__ void dn_mfma(const Args& a, LAS unsigned char* lds, int layer) {
;     seg_to_lds(a, lds, layer);
;     const LAS int* seg = (const LAS int*)(lds + SEG_OFF);
;     pg8::GroupedOrder So{(const char*)(a.ws + WS_HID), (const char*)(a.ws + WS_WDN + (size_t)layer * NE * 1024 * DFF * 2), seg, 4, (int)gridDim.x, (int)blockIdx.x, (size_t)DFF * 2, (size_t)1024 * DFF * 2, (size_t)256 * DFF * 2};
;     EpiDown E{(bf16_t*)(a.ws + WS_YBUF), (const int*)(a.ws + WS_LIST), (const float*)(a.ws + WS_LISTW), seg, lds};
;     pg8::gemm_phase<EpiDown, pg8::GroupedOrder>(lds, DFF, So, E);
; }
.LBB0_1156:
	s_or_b64 exec, exec, s[36:37]
	v_mov_b32_e32 v1, 0x21e80
	ds_read_b32 v2, v1
	s_waitcnt lgkmcnt(0)
	v_readfirstlane_b32 vcc_lo, v2
	s_lshr_b32 vcc_lo, vcc_lo, 6
	s_lshl_b32 vcc_hi, s77, 2
	s_sub_i32 vcc_lo, vcc_lo, vcc_hi
	s_max_i32 vcc_lo, vcc_lo, 0
	s_cmpk_lt_u32 s77, 0xe0
	s_cselect_b32 vcc_lo, 0, vcc_lo
	s_nop 1
	v_writelane_b32 v254, vcc_lo, 63
	s_nop 1
	s_cmp_lt_u32 s61, vcc_lo
	s_cbranch_scc0 .Ldn_entry
	s_mov_b32 vcc_lo, 1
	s_nop 1
	v_writelane_b32 v254, vcc_lo, 62
	s_nop 1
	s_add_u32 s61, s61, vcc_hi
	v_readlane_b32 vcc_lo, v253, 31
	s_nop 1
	s_add_u32 vcc_lo, vcc_lo, vcc_hi
	s_nop 1
	v_writelane_b32 v253, vcc_lo, 31
	s_nop 1
	s_branch .Lgu_restart
